# P3 m1 unit: conv weights (loop invariant) loaded once per unit in front of the causal-conv loop; in-loop reloads and their vmcnt waits removed
# baseline (speedup 1.0000x reference)
.LBB0_586:
	s_or_b64 exec, exec, s[0:1]
	v_or_b32_e32 v32, s90, v136
	v_readlane_b32 s16, v253, 29
	v_lshlrev_b32_e32 v64, 2, v32
	v_readlane_b32 s22, v253, 35
	v_readlane_b32 s23, v253, 36
	s_mov_b64 s[0:1], 0x1000
	s_lshl_b32 s48, s90, 1
	v_lshl_add_u64 v[54:55], s[22:23], 0, v[64:65]
	v_lshl_add_u64 v[56:57], v[54:55], 0, s[0:1]
	s_mov_b64 s[0:1], 0x2000
	v_lshl_add_u64 v[58:59], v[54:55], 0, s[0:1]
	s_mov_b64 s[0:1], 0x3000
	v_lshl_add_u64 v[52:53], v[86:87], 0, s[48:49]
	v_lshl_add_u64 v[60:61], v[54:55], 0, s[0:1]
	global_load_dwordx4 v[194:197], v[54:55], off offset:16
	global_load_dwordx4 v[198:201], v[54:55], off
	global_load_dwordx4 v[202:205], v[56:57], off offset:16
	global_load_dwordx4 v[206:209], v[56:57], off
	global_load_dwordx4 v[210:213], v[58:59], off offset:16
	global_load_dwordx4 v[214:217], v[58:59], off
	global_load_dwordx4 v[218:221], v[60:61], off offset:16
	global_load_dwordx4 v[222:225], v[60:61], off
	s_mov_b32 s48, 0
	s_waitcnt lgkmcnt(0)
	s_barrier
	v_readlane_b32 s17, v253, 30
	v_readlane_b32 s18, v253, 31
	v_readlane_b32 s19, v253, 32
	v_readlane_b32 s20, v253, 33
	v_readlane_b32 s21, v253, 34
	v_readlane_b32 s24, v253, 37
	v_readlane_b32 s25, v253, 38
	v_readlane_b32 s26, v253, 39
	v_readlane_b32 s27, v253, 40
	v_readlane_b32 s28, v253, 41
	v_readlane_b32 s29, v253, 42
	v_readlane_b32 s30, v253, 43
	v_readlane_b32 s31, v253, 44
	s_waitcnt vmcnt(0)
	s_branch .LBB0_588

.LBB0_588:
	v_add_u32_e32 v64, s48, v68
	v_ashrrev_i32_e32 v62, 5, v64
	v_lshl_add_u32 v48, v62, 9, v154
	ds_read_b128 v[32:35], v48 offset:34816
	v_mov_b64_e32 v[36:37], v[194:195]
	v_mov_b64_e32 v[38:39], v[196:197]
	v_mov_b64_e32 v[40:41], v[198:199]
	v_mov_b64_e32 v[42:43], v[200:201]
	s_waitcnt lgkmcnt(0)
	v_lshlrev_b32_e32 v45, 16, v33
	v_lshlrev_b32_e32 v44, 16, v32
	v_and_b32_e32 v33, 0xffff0000, v33
	v_and_b32_e32 v32, 0xffff0000, v32
	v_mov_b32_e32 v47, v42
	v_mov_b32_e32 v42, v41
	v_mov_b32_e32 v46, v40
	v_pk_fma_f32 v[126:127], v[42:43], v[32:33], 0 op_sel_hi:[1,1,0]
	v_lshlrev_b32_e32 v33, 16, v35
	v_lshlrev_b32_e32 v32, 16, v34
	v_mov_b32_e32 v40, v36
	v_mov_b32_e32 v41, v38
	v_pk_fma_f32 v[102:103], v[40:41], v[32:33], 0 op_sel_hi:[1,1,0]
	v_and_b32_e32 v33, 0xffff0000, v35
	v_and_b32_e32 v32, 0xffff0000, v34
	v_mov_b32_e32 v38, v37
	v_pk_fma_f32 v[104:105], v[38:39], v[32:33], 0 op_sel_hi:[1,1,0]
	ds_read_b128 v[36:39], v48 offset:35328
	v_mov_b64_e32 v[32:33], v[202:203]
	v_mov_b64_e32 v[34:35], v[204:205]
	v_mov_b64_e32 v[182:183], v[206:207]
	v_mov_b64_e32 v[184:185], v[208:209]
	v_pk_fma_f32 v[124:125], v[46:47], v[44:45], 0 op_sel_hi:[1,1,0]
	s_waitcnt lgkmcnt(0)
	v_lshlrev_b32_e32 v187, 16, v37
	v_lshlrev_b32_e32 v186, 16, v36
	v_and_b32_e32 v191, 0xffff0000, v37
	v_and_b32_e32 v190, 0xffff0000, v36
	v_lshlrev_b32_e32 v107, 16, v39
	v_lshlrev_b32_e32 v106, 16, v38
	v_and_b32_e32 v111, 0xffff0000, v39
	v_and_b32_e32 v110, 0xffff0000, v38
	ds_read_b128 v[36:39], v48 offset:35840
	s_waitcnt lgkmcnt(0)
	v_lshlrev_b32_e32 v121, 16, v37
	v_lshlrev_b32_e32 v120, 16, v36
	v_and_b32_e32 v119, 0xffff0000, v37
	v_and_b32_e32 v118, 0xffff0000, v36
	v_lshlrev_b32_e32 v113, 16, v39
	v_lshlrev_b32_e32 v112, 16, v38
	v_mov_b32_e32 v108, v32
	v_mov_b32_e32 v109, v34
	v_mov_b32_e32 v34, v33
	v_and_b32_e32 v33, 0xffff0000, v39
	v_and_b32_e32 v32, 0xffff0000, v38
	v_mov_b64_e32 v[36:37], v[210:211]
	v_mov_b64_e32 v[38:39], v[212:213]
	v_mov_b64_e32 v[44:45], v[214:215]
	v_mov_b64_e32 v[46:47], v[216:217]
	ds_read_b128 v[40:43], v48 offset:36352
	v_mov_b32_e32 v188, v182
	v_mov_b32_e32 v189, v184
	v_mov_b32_e32 v184, v183
	v_pk_fma_f32 v[124:125], v[188:189], v[186:187], v[124:125]
	s_waitcnt lgkmcnt(0)
	v_lshlrev_b32_e32 v128, 16, v40
	v_and_b32_e32 v122, 0xffff0000, v40
	v_lshlrev_b32_e32 v129, 16, v41
	v_and_b32_e32 v123, 0xffff0000, v41
	v_lshlrev_b32_e32 v116, 16, v42
	v_and_b32_e32 v114, 0xffff0000, v42
	v_lshlrev_b32_e32 v117, 16, v43
	v_and_b32_e32 v115, 0xffff0000, v43
	v_mov_b64_e32 v[40:41], v[218:219]
	v_mov_b64_e32 v[42:43], v[220:221]
	v_mov_b64_e32 v[48:49], v[222:223]
	v_mov_b64_e32 v[50:51], v[224:225]
	v_pk_fma_f32 v[126:127], v[184:185], v[190:191], v[126:127]
	v_pk_fma_f32 v[34:35], v[34:35], v[110:111], v[104:105]
	v_mov_b32_e32 v182, v44
	v_mov_b32_e32 v183, v46
	v_pk_fma_f32 v[120:121], v[182:183], v[120:121], v[124:125]
	v_mov_b32_e32 v46, v45
	v_pk_fma_f32 v[46:47], v[46:47], v[118:119], v[126:127]
	v_mov_b32_e32 v44, v48
	v_mov_b32_e32 v45, v50
	v_pk_fma_f32 v[44:45], v[44:45], v[128:129], v[120:121]
	v_mov_b32_e32 v50, v49
	v_mul_f32_e32 v48, 0xbfb8aa3b, v44
	v_pk_fma_f32 v[46:47], v[50:51], v[122:123], v[46:47]
	v_fma_f32 v49, v44, s82, -v48
	v_rndne_f32_e32 v50, v48
	v_fmac_f32_e32 v49, 0xb2a5705f, v44
	v_sub_f32_e32 v48, v48, v50
	v_add_f32_e32 v48, v48, v49
	v_exp_f32_e32 v48, v48
	v_cvt_i32_f32_e32 v49, v50
	v_cmp_nlt_f32_e32 vcc, s83, v44
	v_ldexp_f32 v48, v48, v49
	s_nop 0
	v_cndmask_b32_e32 v48, 0, v48, vcc
	v_cmp_ngt_f32_e32 vcc, s84, v44
	s_nop 1
	v_cndmask_b32_e32 v50, v180, v48, vcc
	v_mul_f32_e32 v48, 0xbfb8aa3b, v46
	v_fma_f32 v49, v46, s82, -v48
	v_rndne_f32_e32 v51, v48
	v_fmac_f32_e32 v49, 0xb2a5705f, v46
	v_sub_f32_e32 v48, v48, v51
	v_add_f32_e32 v48, v48, v49
	v_exp_f32_e32 v48, v48
	v_cvt_i32_f32_e32 v49, v51
	v_cmp_nlt_f32_e32 vcc, s83, v46
	v_ldexp_f32 v48, v48, v49
	v_mul_f32_e32 v49, 0xbfb8aa3b, v45
	v_fma_f32 v51, v45, s82, -v49
	v_rndne_f32_e32 v63, v49
	v_fmac_f32_e32 v51, 0xb2a5705f, v45
	v_sub_f32_e32 v49, v49, v63
	v_add_f32_e32 v49, v49, v51
	v_exp_f32_e32 v49, v49
	v_cvt_i32_f32_e32 v51, v63
	v_cndmask_b32_e32 v48, 0, v48, vcc
	v_cmp_ngt_f32_e32 vcc, s84, v46
	v_ldexp_f32 v49, v49, v51
	s_nop 0
	v_cndmask_b32_e32 v48, v180, v48, vcc
	v_cmp_nlt_f32_e32 vcc, s83, v45
	s_nop 1
	v_cndmask_b32_e32 v49, 0, v49, vcc
	v_cmp_ngt_f32_e32 vcc, s84, v45
	s_nop 1
	v_cndmask_b32_e32 v51, v180, v49, vcc
	v_pk_add_f32 v[50:51], v[50:51], 1.0 op_sel_hi:[1,0]
	s_nop 0
	v_div_scale_f32 v49, s[0:1], v51, v51, v45
	v_rcp_f32_e32 v63, v49
	s_nop 0
	v_fma_f32 v99, -v49, v63, 1.0
	v_fmac_f32_e32 v63, v99, v63
	v_div_scale_f32 v99, vcc, v45, v51, v45
	v_mul_f32_e32 v101, v99, v63
	v_fma_f32 v118, -v49, v101, v99
	v_fmac_f32_e32 v101, v118, v63
	v_fma_f32 v49, -v49, v101, v99
	v_div_fmas_f32 v49, v49, v63, v101
	v_div_fixup_f32 v45, v49, v51, v45
	v_div_scale_f32 v49, s[0:1], v50, v50, v44
	v_rcp_f32_e32 v51, v49
	s_nop 0
	v_fma_f32 v63, -v49, v51, 1.0
	v_fmac_f32_e32 v51, v63, v51
	v_div_scale_f32 v63, vcc, v44, v50, v44
	v_mul_f32_e32 v99, v63, v51
	v_fma_f32 v101, -v49, v99, v63
	v_fmac_f32_e32 v99, v101, v51
	v_fma_f32 v49, -v49, v99, v63
	v_div_fmas_f32 v49, v49, v51, v99
	v_div_fixup_f32 v44, v49, v50, v44
	v_mul_f32_e32 v49, 0xbfb8aa3b, v47
	v_fma_f32 v50, v47, s82, -v49
	v_rndne_f32_e32 v51, v49
	v_fmac_f32_e32 v50, 0xb2a5705f, v47
	v_sub_f32_e32 v49, v49, v51
	v_add_f32_e32 v49, v49, v50
	v_exp_f32_e32 v49, v49
	v_cvt_i32_f32_e32 v50, v51
	v_cmp_nlt_f32_e32 vcc, s83, v47
	v_pk_mul_f32 v[44:45], v[66:67], v[44:45]
	v_ldexp_f32 v49, v49, v50
	v_cndmask_b32_e32 v49, 0, v49, vcc
	v_cmp_ngt_f32_e32 vcc, s84, v47
	s_nop 1
	v_cndmask_b32_e32 v49, v180, v49, vcc
	v_pk_add_f32 v[48:49], v[48:49], 1.0 op_sel_hi:[1,0]
	s_nop 0
	v_div_scale_f32 v50, s[0:1], v49, v49, v47
	v_rcp_f32_e32 v51, v50
	s_nop 0
	v_fma_f32 v63, -v50, v51, 1.0
	v_fmac_f32_e32 v51, v63, v51
	v_div_scale_f32 v63, vcc, v47, v49, v47
	v_mul_f32_e32 v99, v63, v51
	v_fma_f32 v101, -v50, v99, v63
	v_fmac_f32_e32 v99, v101, v51
	v_fma_f32 v50, -v50, v99, v63
	v_div_fmas_f32 v50, v50, v51, v99
	v_div_fixup_f32 v47, v50, v49, v47
	v_div_scale_f32 v49, s[0:1], v48, v48, v46
	v_rcp_f32_e32 v50, v49
	s_nop 0
	v_fma_f32 v51, -v49, v50, 1.0
	v_fmac_f32_e32 v50, v51, v50
	v_div_scale_f32 v51, vcc, v46, v48, v46
	v_mul_f32_e32 v63, v51, v50
	v_fma_f32 v99, -v49, v63, v51
	v_fmac_f32_e32 v63, v99, v50
	v_fma_f32 v49, -v49, v63, v51
	v_div_fmas_f32 v49, v49, v50, v63
	v_div_fixup_f32 v46, v49, v48, v46
	v_pk_fma_f32 v[48:49], v[108:109], v[106:107], v[102:103]
	v_mov_b32_e32 v50, v36
	v_mov_b32_e32 v51, v38
	v_mov_b32_e32 v38, v37
	v_pk_fma_f32 v[48:49], v[50:51], v[112:113], v[48:49]
	v_pk_fma_f32 v[32:33], v[38:39], v[32:33], v[34:35]
	v_mov_b32_e32 v34, v40
	v_mov_b32_e32 v35, v42
	v_pk_fma_f32 v[34:35], v[34:35], v[116:117], v[48:49]
	v_mov_b32_e32 v42, v41
	v_mul_f32_e32 v36, 0xbfb8aa3b, v34
	v_fma_f32 v37, v34, s82, -v36
	v_rndne_f32_e32 v38, v36
	v_fmac_f32_e32 v37, 0xb2a5705f, v34
	v_sub_f32_e32 v36, v36, v38
	v_add_f32_e32 v36, v36, v37
	v_exp_f32_e32 v36, v36
	v_cvt_i32_f32_e32 v37, v38
	v_pk_fma_f32 v[32:33], v[42:43], v[114:115], v[32:33]
	v_cmp_nlt_f32_e32 vcc, s83, v34
	v_pk_mul_f32 v[46:47], v[66:67], v[46:47]
	v_ldexp_f32 v36, v36, v37
	v_mul_f32_e32 v37, 0xbfb8aa3b, v32
	v_fma_f32 v38, v32, s82, -v37
	v_rndne_f32_e32 v39, v37
	v_fmac_f32_e32 v38, 0xb2a5705f, v32
	v_sub_f32_e32 v37, v37, v39
	v_add_f32_e32 v37, v37, v38
	v_exp_f32_e32 v37, v37
	v_cvt_i32_f32_e32 v38, v39
	v_cndmask_b32_e32 v36, 0, v36, vcc
	v_cmp_ngt_f32_e32 vcc, s84, v34
	v_ashrrev_i32_e32 v63, 31, v62
	v_ldexp_f32 v37, v37, v38
	v_cndmask_b32_e32 v36, v180, v36, vcc
	v_cmp_nlt_f32_e32 vcc, s83, v32
	s_nop 1
	v_cndmask_b32_e32 v37, 0, v37, vcc
	v_cmp_ngt_f32_e32 vcc, s84, v32
	s_nop 1
	v_cndmask_b32_e32 v38, v180, v37, vcc
	v_mul_f32_e32 v37, 0xbfb8aa3b, v35
	v_fma_f32 v39, v35, s82, -v37
	v_rndne_f32_e32 v40, v37
	v_fmac_f32_e32 v39, 0xb2a5705f, v35
	v_sub_f32_e32 v37, v37, v40
	v_add_f32_e32 v37, v37, v39
	v_exp_f32_e32 v37, v37
	v_cvt_i32_f32_e32 v39, v40
	v_cmp_nlt_f32_e32 vcc, s83, v35
	v_ldexp_f32 v37, v37, v39
	s_nop 0
	v_cndmask_b32_e32 v37, 0, v37, vcc
	v_cmp_ngt_f32_e32 vcc, s84, v35
	s_nop 1
	v_cndmask_b32_e32 v37, v180, v37, vcc
	v_pk_add_f32 v[36:37], v[36:37], 1.0 op_sel_hi:[1,0]
	s_nop 0
	v_div_scale_f32 v39, s[0:1], v37, v37, v35
	v_rcp_f32_e32 v40, v39
	s_nop 0
	v_fma_f32 v41, -v39, v40, 1.0
	v_fmac_f32_e32 v40, v41, v40
	v_div_scale_f32 v41, vcc, v35, v37, v35
	v_mul_f32_e32 v42, v41, v40
	v_fma_f32 v43, -v39, v42, v41
	v_fmac_f32_e32 v42, v43, v40
	v_fma_f32 v39, -v39, v42, v41
	v_div_fmas_f32 v39, v39, v40, v42
	v_div_fixup_f32 v35, v39, v37, v35
	v_div_scale_f32 v37, s[0:1], v36, v36, v34
	v_rcp_f32_e32 v39, v37
	s_nop 0
	v_fma_f32 v40, -v37, v39, 1.0
	v_fmac_f32_e32 v39, v40, v39
	v_div_scale_f32 v40, vcc, v34, v36, v34
	v_mul_f32_e32 v41, v40, v39
	v_fma_f32 v42, -v37, v41, v40
	v_fmac_f32_e32 v41, v42, v39
	v_fma_f32 v37, -v37, v41, v40
	v_div_fmas_f32 v37, v37, v39, v41
	v_div_fixup_f32 v34, v37, v36, v34
	v_mul_f32_e32 v36, 0xbfb8aa3b, v33
	v_fma_f32 v37, v33, s82, -v36
	v_rndne_f32_e32 v39, v36
	v_fmac_f32_e32 v37, 0xb2a5705f, v33
	v_sub_f32_e32 v36, v36, v39
	v_add_f32_e32 v36, v36, v37
	v_exp_f32_e32 v36, v36
	v_cvt_i32_f32_e32 v37, v39
	v_cmp_nlt_f32_e32 vcc, s83, v33
	v_pk_mul_f32 v[34:35], v[66:67], v[34:35]
	v_ldexp_f32 v36, v36, v37
	v_cndmask_b32_e32 v36, 0, v36, vcc
	v_cmp_ngt_f32_e32 vcc, s84, v33
	v_bfe_u32 v43, v35, 16, 1
	v_add3_u32 v43, v35, v43, s89
	v_cndmask_b32_e32 v39, v180, v36, vcc
	v_pk_add_f32 v[36:37], v[38:39], 1.0 op_sel_hi:[1,0]
	s_nop 0
	v_div_scale_f32 v38, s[0:1], v37, v37, v33
	v_rcp_f32_e32 v39, v38
	s_nop 0
	v_fma_f32 v40, -v38, v39, 1.0
	v_fmac_f32_e32 v39, v40, v39
	v_div_scale_f32 v40, vcc, v33, v37, v33
	v_mul_f32_e32 v41, v40, v39
	v_fma_f32 v42, -v38, v41, v40
	v_fmac_f32_e32 v41, v42, v39
	v_fma_f32 v38, -v38, v41, v40
	v_div_fmas_f32 v38, v38, v39, v41
	v_div_fixup_f32 v33, v38, v37, v33
	v_div_scale_f32 v37, s[0:1], v36, v36, v32
	v_rcp_f32_e32 v38, v37
	v_bfe_u32 v42, v34, 16, 1
	v_add3_u32 v42, v34, v42, s89
	v_fma_f32 v39, -v37, v38, 1.0
	v_fmac_f32_e32 v38, v39, v38
	v_div_scale_f32 v39, vcc, v32, v36, v32
	v_mul_f32_e32 v40, v39, v38
	v_fma_f32 v41, -v37, v40, v39
	v_fmac_f32_e32 v40, v41, v38
	v_fma_f32 v37, -v37, v40, v39
	v_div_fmas_f32 v37, v37, v38, v40
	v_div_fixup_f32 v32, v37, v36, v32
	v_bfe_u32 v38, v47, 16, 1
	v_bfe_u32 v39, v46, 16, 1
	v_pk_mul_f32 v[32:33], v[66:67], v[32:33]
	v_add3_u32 v40, v46, v39, s89
	v_add3_u32 v41, v47, v38, s89
	v_bfe_u32 v38, v44, 16, 1
	v_bfe_u32 v39, v45, 16, 1
	v_bfe_u32 v36, v33, 16, 1
	v_bfe_u32 v37, v32, 16, 1
	v_add3_u32 v39, v45, v39, s89
	v_add3_u32 v38, v44, v38, s89
	v_add3_u32 v37, v32, v37, s89
	v_add3_u32 v36, v33, v36, s89
	v_lshrrev_b32_e32 v48, 16, v38
	v_lshrrev_b32_e32 v49, 16, v39
	v_lshrrev_b32_e32 v38, 16, v42
	v_lshrrev_b32_e32 v39, 16, v43
	v_and_or_b32 v39, v36, s88, v39
	v_and_or_b32 v38, v37, s88, v38
	v_and_or_b32 v37, v41, s88, v49
	v_and_or_b32 v36, v40, s88, v48
	v_lshl_add_u64 v[40:41], s[62:63], 0, v[62:63]
	v_lshlrev_b64 v[40:41], 10, v[40:41]
	v_lshl_add_u64 v[40:41], v[52:53], 0, v[40:41]
	global_store_dwordx4 v[40:41], v[36:39], off
	s_and_saveexec_b64 s[0:1], s[14:15]
	s_cbranch_execz .LBB0_590
	v_lshl_add_u32 v36, v62, 2, s69
	ds_read_b32 v36, v36 offset:1024
	s_waitcnt lgkmcnt(0)
	v_pk_mul_f32 v[40:41], v[46:47], v[36:37] op_sel_hi:[1,0]
	v_pk_mul_f32 v[32:33], v[32:33], v[36:37] op_sel_hi:[1,0]
	v_pk_mul_f32 v[38:39], v[44:45], v[36:37] op_sel_hi:[1,0]
	v_pk_mul_f32 v[34:35], v[34:35], v[36:37] op_sel_hi:[1,0]
	v_bfe_u32 v36, v33, 16, 1
	v_bfe_u32 v37, v32, 16, 1
	v_bfe_u32 v42, v41, 16, 1
	v_bfe_u32 v43, v40, 16, 1
	v_add3_u32 v40, v40, v43, s89
	v_add3_u32 v41, v41, v42, s89
	v_add3_u32 v32, v32, v37, s89
	v_add3_u32 v33, v33, v36, s89
	v_bfe_u32 v36, v38, 16, 1
	v_bfe_u32 v37, v39, 16, 1
	v_bfe_u32 v42, v34, 16, 1
	v_bfe_u32 v43, v35, 16, 1
	v_add3_u32 v35, v35, v43, s89
	v_add3_u32 v34, v34, v42, s89
	v_add3_u32 v37, v39, v37, s89
	v_add3_u32 v36, v38, v36, s89
	v_lshrrev_b32_e32 v36, 16, v36
	v_lshrrev_b32_e32 v37, 16, v37
	v_lshrrev_b32_e32 v34, 16, v34
	v_lshrrev_b32_e32 v35, 16, v35
	v_and_or_b32 v35, v33, s88, v35
	v_and_or_b32 v34, v32, s88, v34
	v_and_or_b32 v33, v41, s88, v37
	v_and_or_b32 v32, v40, s88, v36
	v_mad_u64_u32 v[36:37], s[64:65], v62, s33, v[88:89]
	ds_write_b128 v36, v[32:35]
.LBB0_590:
	s_or_b64 exec, exec, s[0:1]
	v_add_u32_e32 v32, 0x200, v64
	v_ashrrev_i32_e32 v62, 5, v32
	v_lshl_add_u32 v48, v62, 9, v154
	ds_read_b128 v[32:35], v48 offset:34816
	v_mov_b64_e32 v[36:37], v[194:195]
	v_mov_b64_e32 v[38:39], v[196:197]
	v_mov_b64_e32 v[40:41], v[198:199]
	v_mov_b64_e32 v[42:43], v[200:201]
	s_waitcnt lgkmcnt(0)
	v_lshlrev_b32_e32 v45, 16, v33
	v_lshlrev_b32_e32 v44, 16, v32
	v_and_b32_e32 v33, 0xffff0000, v33
	v_and_b32_e32 v32, 0xffff0000, v32
	v_mov_b32_e32 v47, v42
	v_mov_b32_e32 v42, v41
	v_mov_b32_e32 v46, v40
	v_pk_fma_f32 v[126:127], v[42:43], v[32:33], 0 op_sel_hi:[1,1,0]
	v_lshlrev_b32_e32 v33, 16, v35
	v_lshlrev_b32_e32 v32, 16, v34
	v_mov_b32_e32 v40, v36
	v_mov_b32_e32 v41, v38
	v_pk_fma_f32 v[102:103], v[40:41], v[32:33], 0 op_sel_hi:[1,1,0]
	v_and_b32_e32 v33, 0xffff0000, v35
	v_and_b32_e32 v32, 0xffff0000, v34
	v_mov_b32_e32 v38, v37
	v_pk_fma_f32 v[104:105], v[38:39], v[32:33], 0 op_sel_hi:[1,1,0]
	ds_read_b128 v[36:39], v48 offset:35328
	v_mov_b64_e32 v[32:33], v[202:203]
	v_mov_b64_e32 v[34:35], v[204:205]
	v_mov_b64_e32 v[182:183], v[206:207]
	v_mov_b64_e32 v[184:185], v[208:209]
	v_pk_fma_f32 v[124:125], v[46:47], v[44:45], 0 op_sel_hi:[1,1,0]
	s_waitcnt lgkmcnt(0)
	v_lshlrev_b32_e32 v187, 16, v37
	v_lshlrev_b32_e32 v186, 16, v36
	v_and_b32_e32 v191, 0xffff0000, v37
	v_and_b32_e32 v190, 0xffff0000, v36
	v_lshlrev_b32_e32 v107, 16, v39
	v_lshlrev_b32_e32 v106, 16, v38
	v_and_b32_e32 v111, 0xffff0000, v39
	v_and_b32_e32 v110, 0xffff0000, v38
	ds_read_b128 v[36:39], v48 offset:35840
	s_waitcnt lgkmcnt(0)
	v_lshlrev_b32_e32 v121, 16, v37
	v_lshlrev_b32_e32 v120, 16, v36
	v_and_b32_e32 v119, 0xffff0000, v37
	v_and_b32_e32 v118, 0xffff0000, v36
	v_lshlrev_b32_e32 v113, 16, v39
	v_lshlrev_b32_e32 v112, 16, v38
	v_mov_b32_e32 v108, v32
	v_mov_b32_e32 v109, v34
	v_mov_b32_e32 v34, v33
	v_and_b32_e32 v33, 0xffff0000, v39
	v_and_b32_e32 v32, 0xffff0000, v38
	v_mov_b64_e32 v[36:37], v[210:211]
	v_mov_b64_e32 v[38:39], v[212:213]
	v_mov_b64_e32 v[44:45], v[214:215]
	v_mov_b64_e32 v[46:47], v[216:217]
	ds_read_b128 v[40:43], v48 offset:36352
	v_mov_b32_e32 v188, v182
	v_mov_b32_e32 v189, v184
	v_mov_b32_e32 v184, v183
	v_pk_fma_f32 v[124:125], v[188:189], v[186:187], v[124:125]
	s_waitcnt lgkmcnt(0)
	v_lshlrev_b32_e32 v128, 16, v40
	v_and_b32_e32 v122, 0xffff0000, v40
	v_lshlrev_b32_e32 v129, 16, v41
	v_and_b32_e32 v123, 0xffff0000, v41
	v_lshlrev_b32_e32 v116, 16, v42
	v_and_b32_e32 v114, 0xffff0000, v42
	v_lshlrev_b32_e32 v117, 16, v43
	v_and_b32_e32 v115, 0xffff0000, v43
	v_mov_b64_e32 v[40:41], v[218:219]
	v_mov_b64_e32 v[42:43], v[220:221]
	v_mov_b64_e32 v[48:49], v[222:223]
	v_mov_b64_e32 v[50:51], v[224:225]
	v_pk_fma_f32 v[126:127], v[184:185], v[190:191], v[126:127]
	v_pk_fma_f32 v[34:35], v[34:35], v[110:111], v[104:105]
	v_mov_b32_e32 v182, v44
	v_mov_b32_e32 v183, v46
	v_pk_fma_f32 v[120:121], v[182:183], v[120:121], v[124:125]
	v_mov_b32_e32 v46, v45
	v_pk_fma_f32 v[46:47], v[46:47], v[118:119], v[126:127]
	v_mov_b32_e32 v44, v48
	v_mov_b32_e32 v45, v50
	v_pk_fma_f32 v[44:45], v[44:45], v[128:129], v[120:121]
	v_mov_b32_e32 v50, v49
	v_mul_f32_e32 v48, 0xbfb8aa3b, v44
	v_pk_fma_f32 v[46:47], v[50:51], v[122:123], v[46:47]
	v_fma_f32 v49, v44, s82, -v48
	v_rndne_f32_e32 v50, v48
	v_fmac_f32_e32 v49, 0xb2a5705f, v44
	v_sub_f32_e32 v48, v48, v50
	v_add_f32_e32 v48, v48, v49
	v_exp_f32_e32 v48, v48
	v_cvt_i32_f32_e32 v49, v50
	v_cmp_nlt_f32_e32 vcc, s83, v44
	v_ldexp_f32 v48, v48, v49
	s_nop 0
	v_cndmask_b32_e32 v48, 0, v48, vcc
	v_cmp_ngt_f32_e32 vcc, s84, v44
	s_nop 1
	v_cndmask_b32_e32 v50, v180, v48, vcc
	v_mul_f32_e32 v48, 0xbfb8aa3b, v46
	v_fma_f32 v49, v46, s82, -v48
	v_rndne_f32_e32 v51, v48
	v_fmac_f32_e32 v49, 0xb2a5705f, v46
	v_sub_f32_e32 v48, v48, v51
	v_add_f32_e32 v48, v48, v49
	v_exp_f32_e32 v48, v48
	v_cvt_i32_f32_e32 v49, v51
	v_cmp_nlt_f32_e32 vcc, s83, v46
	v_ldexp_f32 v48, v48, v49
	v_mul_f32_e32 v49, 0xbfb8aa3b, v45
	v_fma_f32 v51, v45, s82, -v49
	v_rndne_f32_e32 v63, v49
	v_fmac_f32_e32 v51, 0xb2a5705f, v45
	v_sub_f32_e32 v49, v49, v63
	v_add_f32_e32 v49, v49, v51
	v_exp_f32_e32 v49, v49
	v_cvt_i32_f32_e32 v51, v63
	v_cndmask_b32_e32 v48, 0, v48, vcc
	v_cmp_ngt_f32_e32 vcc, s84, v46
	v_ldexp_f32 v49, v49, v51
	s_nop 0
	v_cndmask_b32_e32 v48, v180, v48, vcc
	v_cmp_nlt_f32_e32 vcc, s83, v45
	s_nop 1
	v_cndmask_b32_e32 v49, 0, v49, vcc
	v_cmp_ngt_f32_e32 vcc, s84, v45
	s_nop 1
	v_cndmask_b32_e32 v51, v180, v49, vcc
	v_pk_add_f32 v[50:51], v[50:51], 1.0 op_sel_hi:[1,0]
	s_nop 0
	v_div_scale_f32 v49, s[0:1], v51, v51, v45
	v_rcp_f32_e32 v63, v49
	s_nop 0
	v_fma_f32 v64, -v49, v63, 1.0
	v_fmac_f32_e32 v63, v64, v63
	v_div_scale_f32 v64, vcc, v45, v51, v45
	v_mul_f32_e32 v99, v64, v63
	v_fma_f32 v101, -v49, v99, v64
	v_fmac_f32_e32 v99, v101, v63
	v_fma_f32 v49, -v49, v99, v64
	v_div_fmas_f32 v49, v49, v63, v99
	v_div_fixup_f32 v45, v49, v51, v45
	v_div_scale_f32 v49, s[0:1], v50, v50, v44
	v_rcp_f32_e32 v51, v49
	s_nop 0
	v_fma_f32 v63, -v49, v51, 1.0
	v_fmac_f32_e32 v51, v63, v51
	v_div_scale_f32 v63, vcc, v44, v50, v44
	v_mul_f32_e32 v64, v63, v51
	v_fma_f32 v99, -v49, v64, v63
	v_fmac_f32_e32 v64, v99, v51
	v_fma_f32 v49, -v49, v64, v63
	v_div_fmas_f32 v49, v49, v51, v64
	v_div_fixup_f32 v44, v49, v50, v44
	v_mul_f32_e32 v49, 0xbfb8aa3b, v47
	v_fma_f32 v50, v47, s82, -v49
	v_rndne_f32_e32 v51, v49
	v_fmac_f32_e32 v50, 0xb2a5705f, v47
	v_sub_f32_e32 v49, v49, v51
	v_add_f32_e32 v49, v49, v50
	v_exp_f32_e32 v49, v49
	v_cvt_i32_f32_e32 v50, v51
	v_cmp_nlt_f32_e32 vcc, s83, v47
	v_pk_mul_f32 v[44:45], v[66:67], v[44:45]
	v_ldexp_f32 v49, v49, v50
	v_cndmask_b32_e32 v49, 0, v49, vcc
	v_cmp_ngt_f32_e32 vcc, s84, v47
	s_nop 1
	v_cndmask_b32_e32 v49, v180, v49, vcc
	v_pk_add_f32 v[48:49], v[48:49], 1.0 op_sel_hi:[1,0]
	s_nop 0
	v_div_scale_f32 v50, s[0:1], v49, v49, v47
	v_rcp_f32_e32 v51, v50
	s_nop 0
	v_fma_f32 v63, -v50, v51, 1.0
	v_fmac_f32_e32 v51, v63, v51
	v_div_scale_f32 v63, vcc, v47, v49, v47
	v_mul_f32_e32 v64, v63, v51
	v_fma_f32 v99, -v50, v64, v63
	v_fmac_f32_e32 v64, v99, v51
	v_fma_f32 v50, -v50, v64, v63
	v_div_fmas_f32 v50, v50, v51, v64
	v_div_fixup_f32 v47, v50, v49, v47
	v_div_scale_f32 v49, s[0:1], v48, v48, v46
	v_rcp_f32_e32 v50, v49
	s_nop 0
	v_fma_f32 v51, -v49, v50, 1.0
	v_fmac_f32_e32 v50, v51, v50
	v_div_scale_f32 v51, vcc, v46, v48, v46
	v_mul_f32_e32 v63, v51, v50
	v_fma_f32 v64, -v49, v63, v51
	v_fmac_f32_e32 v63, v64, v50
	v_fma_f32 v49, -v49, v63, v51
	v_div_fmas_f32 v49, v49, v50, v63
	v_div_fixup_f32 v46, v49, v48, v46
	v_pk_fma_f32 v[48:49], v[108:109], v[106:107], v[102:103]
	v_mov_b32_e32 v50, v36
	v_mov_b32_e32 v51, v38
	v_mov_b32_e32 v38, v37
	v_pk_fma_f32 v[48:49], v[50:51], v[112:113], v[48:49]
	v_pk_fma_f32 v[32:33], v[38:39], v[32:33], v[34:35]
	v_mov_b32_e32 v34, v40
	v_mov_b32_e32 v35, v42
	v_pk_fma_f32 v[34:35], v[34:35], v[116:117], v[48:49]
	v_mov_b32_e32 v42, v41
	v_mul_f32_e32 v36, 0xbfb8aa3b, v34
	v_fma_f32 v37, v34, s82, -v36
	v_rndne_f32_e32 v38, v36
	v_fmac_f32_e32 v37, 0xb2a5705f, v34
	v_sub_f32_e32 v36, v36, v38
	v_add_f32_e32 v36, v36, v37
	v_exp_f32_e32 v36, v36
	v_cvt_i32_f32_e32 v37, v38
	v_pk_fma_f32 v[32:33], v[42:43], v[114:115], v[32:33]
	v_cmp_nlt_f32_e32 vcc, s83, v34
	v_pk_mul_f32 v[46:47], v[66:67], v[46:47]
	v_ldexp_f32 v36, v36, v37
	v_mul_f32_e32 v37, 0xbfb8aa3b, v32
	v_fma_f32 v38, v32, s82, -v37
	v_rndne_f32_e32 v39, v37
	v_fmac_f32_e32 v38, 0xb2a5705f, v32
	v_sub_f32_e32 v37, v37, v39
	v_add_f32_e32 v37, v37, v38
	v_exp_f32_e32 v37, v37
	v_cvt_i32_f32_e32 v38, v39
	v_cndmask_b32_e32 v36, 0, v36, vcc
	v_cmp_ngt_f32_e32 vcc, s84, v34
	v_ashrrev_i32_e32 v63, 31, v62
	v_ldexp_f32 v37, v37, v38
	v_cndmask_b32_e32 v36, v180, v36, vcc
	v_cmp_nlt_f32_e32 vcc, s83, v32
	s_nop 1
	v_cndmask_b32_e32 v37, 0, v37, vcc
	v_cmp_ngt_f32_e32 vcc, s84, v32
	s_nop 1
	v_cndmask_b32_e32 v38, v180, v37, vcc
	v_mul_f32_e32 v37, 0xbfb8aa3b, v35
	v_fma_f32 v39, v35, s82, -v37
	v_rndne_f32_e32 v40, v37
	v_fmac_f32_e32 v39, 0xb2a5705f, v35
	v_sub_f32_e32 v37, v37, v40
	v_add_f32_e32 v37, v37, v39
	v_exp_f32_e32 v37, v37
	v_cvt_i32_f32_e32 v39, v40
	v_cmp_nlt_f32_e32 vcc, s83, v35
	v_ldexp_f32 v37, v37, v39
	s_nop 0
	v_cndmask_b32_e32 v37, 0, v37, vcc
	v_cmp_ngt_f32_e32 vcc, s84, v35
	s_nop 1
	v_cndmask_b32_e32 v37, v180, v37, vcc
	v_pk_add_f32 v[36:37], v[36:37], 1.0 op_sel_hi:[1,0]
	s_nop 0
	v_div_scale_f32 v39, s[0:1], v37, v37, v35
	v_rcp_f32_e32 v40, v39
	s_nop 0
	v_fma_f32 v41, -v39, v40, 1.0
	v_fmac_f32_e32 v40, v41, v40
	v_div_scale_f32 v41, vcc, v35, v37, v35
	v_mul_f32_e32 v42, v41, v40
	v_fma_f32 v43, -v39, v42, v41
	v_fmac_f32_e32 v42, v43, v40
	v_fma_f32 v39, -v39, v42, v41
	v_div_fmas_f32 v39, v39, v40, v42
	v_div_fixup_f32 v35, v39, v37, v35
	v_div_scale_f32 v37, s[0:1], v36, v36, v34
	v_rcp_f32_e32 v39, v37
	s_nop 0
	v_fma_f32 v40, -v37, v39, 1.0
	v_fmac_f32_e32 v39, v40, v39
	v_div_scale_f32 v40, vcc, v34, v36, v34
	v_mul_f32_e32 v41, v40, v39
	v_fma_f32 v42, -v37, v41, v40
	v_fmac_f32_e32 v41, v42, v39
	v_fma_f32 v37, -v37, v41, v40
	v_div_fmas_f32 v37, v37, v39, v41
	v_div_fixup_f32 v34, v37, v36, v34
	v_mul_f32_e32 v36, 0xbfb8aa3b, v33
	v_fma_f32 v37, v33, s82, -v36
	v_rndne_f32_e32 v39, v36
	v_fmac_f32_e32 v37, 0xb2a5705f, v33
	v_sub_f32_e32 v36, v36, v39
	v_add_f32_e32 v36, v36, v37
	v_exp_f32_e32 v36, v36
	v_cvt_i32_f32_e32 v37, v39
	v_cmp_nlt_f32_e32 vcc, s83, v33
	v_pk_mul_f32 v[34:35], v[66:67], v[34:35]
	v_ldexp_f32 v36, v36, v37
	v_cndmask_b32_e32 v36, 0, v36, vcc
	v_cmp_ngt_f32_e32 vcc, s84, v33
	v_bfe_u32 v43, v35, 16, 1
	v_add3_u32 v43, v35, v43, s89
	v_cndmask_b32_e32 v39, v180, v36, vcc
	v_pk_add_f32 v[36:37], v[38:39], 1.0 op_sel_hi:[1,0]
	s_nop 0
	v_div_scale_f32 v38, s[0:1], v37, v37, v33
	v_rcp_f32_e32 v39, v38
	s_nop 0
	v_fma_f32 v40, -v38, v39, 1.0
	v_fmac_f32_e32 v39, v40, v39
	v_div_scale_f32 v40, vcc, v33, v37, v33
	v_mul_f32_e32 v41, v40, v39
	v_fma_f32 v42, -v38, v41, v40
	v_fmac_f32_e32 v41, v42, v39
	v_fma_f32 v38, -v38, v41, v40
	v_div_fmas_f32 v38, v38, v39, v41
	v_div_fixup_f32 v33, v38, v37, v33
	v_div_scale_f32 v37, s[0:1], v36, v36, v32
	v_rcp_f32_e32 v38, v37
	v_bfe_u32 v42, v34, 16, 1
	v_add3_u32 v42, v34, v42, s89
	v_fma_f32 v39, -v37, v38, 1.0
	v_fmac_f32_e32 v38, v39, v38
	v_div_scale_f32 v39, vcc, v32, v36, v32
	v_mul_f32_e32 v40, v39, v38
	v_fma_f32 v41, -v37, v40, v39
	v_fmac_f32_e32 v40, v41, v38
	v_fma_f32 v37, -v37, v40, v39
	v_div_fmas_f32 v37, v37, v38, v40
	v_div_fixup_f32 v32, v37, v36, v32
	v_bfe_u32 v38, v47, 16, 1
	v_bfe_u32 v39, v46, 16, 1
	v_pk_mul_f32 v[32:33], v[66:67], v[32:33]
	v_add3_u32 v40, v46, v39, s89
	v_add3_u32 v41, v47, v38, s89
	v_bfe_u32 v38, v44, 16, 1
	v_bfe_u32 v39, v45, 16, 1
	v_bfe_u32 v36, v33, 16, 1
	v_bfe_u32 v37, v32, 16, 1
	v_add3_u32 v39, v45, v39, s89
	v_add3_u32 v38, v44, v38, s89
	v_add3_u32 v37, v32, v37, s89
	v_add3_u32 v36, v33, v36, s89
	v_lshrrev_b32_e32 v48, 16, v38
	v_lshrrev_b32_e32 v49, 16, v39
	v_lshrrev_b32_e32 v38, 16, v42
	v_lshrrev_b32_e32 v39, 16, v43
	v_and_or_b32 v39, v36, s88, v39
	v_and_or_b32 v38, v37, s88, v38
	v_and_or_b32 v37, v41, s88, v49
	v_and_or_b32 v36, v40, s88, v48
	v_lshl_add_u64 v[40:41], s[62:63], 0, v[62:63]
	v_lshlrev_b64 v[40:41], 10, v[40:41]
	v_lshl_add_u64 v[40:41], v[52:53], 0, v[40:41]
	global_store_dwordx4 v[40:41], v[36:39], off
	s_and_saveexec_b64 s[0:1], s[14:15]
	s_cbranch_execz .LBB0_587
	v_lshl_add_u32 v36, v62, 2, s69
	ds_read_b32 v36, v36 offset:1024
	s_waitcnt lgkmcnt(0)
	v_pk_mul_f32 v[40:41], v[46:47], v[36:37] op_sel_hi:[1,0]
	v_pk_mul_f32 v[32:33], v[32:33], v[36:37] op_sel_hi:[1,0]
	v_pk_mul_f32 v[38:39], v[44:45], v[36:37] op_sel_hi:[1,0]
	v_pk_mul_f32 v[34:35], v[34:35], v[36:37] op_sel_hi:[1,0]
	v_bfe_u32 v36, v33, 16, 1
	v_bfe_u32 v37, v32, 16, 1
	v_bfe_u32 v42, v41, 16, 1
	v_bfe_u32 v43, v40, 16, 1
	v_add3_u32 v40, v40, v43, s89
	v_add3_u32 v41, v41, v42, s89
	v_add3_u32 v32, v32, v37, s89
	v_add3_u32 v33, v33, v36, s89
	v_bfe_u32 v36, v38, 16, 1
	v_bfe_u32 v37, v39, 16, 1
	v_bfe_u32 v42, v34, 16, 1
	v_bfe_u32 v43, v35, 16, 1
	v_add3_u32 v35, v35, v43, s89
	v_add3_u32 v34, v34, v42, s89
	v_add3_u32 v37, v39, v37, s89
	v_add3_u32 v36, v38, v36, s89
	v_lshrrev_b32_e32 v36, 16, v36
	v_lshrrev_b32_e32 v37, 16, v37
	v_lshrrev_b32_e32 v34, 16, v34
	v_lshrrev_b32_e32 v35, 16, v35
	v_and_or_b32 v35, v33, s88, v35
	v_and_or_b32 v34, v32, s88, v34
	v_and_or_b32 v33, v41, s88, v37
	v_and_or_b32 v32, v40, s88, v36
	v_mad_u64_u32 v[36:37], s[64:65], v62, s33, v[88:89]
	ds_write_b128 v36, v[32:35]
	s_branch .LBB0_587
